# v032-bsort-five-slots
# speedup vs baseline: 1.1337x; 1.0071x over previous
_Z7k_bsortPK15HIP_vector_typeIfLj2EEPKiS4_PS_IfLj4EEPi:
	s_load_dwordx4 s[20:23], s[0:1], 0x0
	s_movk_i32 s3, 0x80
	v_cmp_gt_u32_e64 s[4:5], s3, v0
	v_lshlrev_b32_e32 v10, 2, v0
	s_and_saveexec_b64 s[6:7], s[4:5]
	v_mov_b32_e32 v1, 0
	ds_write_b32 v10, v1
	s_or_b64 exec, exec, s[6:7]
	s_ashr_i32 s3, s2, 31
	s_lshl_b64 s[6:7], s[2:3], 2
	s_waitcnt lgkmcnt(0)
	s_add_u32 s6, s22, s6
	s_addc_u32 s7, s23, s7
	s_load_dwordx2 s[14:15], s[6:7], 0x0
	s_load_dwordx2 s[28:29], s[0:1], 0x10
	s_mov_b64 s[8:9], -1
	s_waitcnt lgkmcnt(0)
	s_barrier
	s_sub_i32 s3, s15, s14
	s_cmpk_gt_i32 s3, 0xa00
	s_cselect_b64 s[6:7], -1, 0
	s_cmpk_lt_i32 s3, 0xa01
	v_add_u32_e32 v20, s14, v0
	s_cbranch_scc1 .LBB2_22
	s_mov_b32 s10, 0
	v_mov_b32_e32 v1, 1
	s_branch .LBB2_5

.LBB2_31:
	s_or_b64 exec, exec, s[0:1]
	v_or_b32_e32 v1, 0x800, v0
	v_cmp_gt_i32_e64 s[50:51], s3, v1
	v_mov_b32_e32 v64, 0
	v_mov_b32_e32 v65, 0
	s_and_saveexec_b64 s[0:1], s[50:51]
	s_cbranch_execz .Lbs5_ld
	v_add_u32_e32 v64, s14, v1
	v_ashrrev_i32_e32 v65, 31, v64
	v_lshl_add_u64 v[64:65], v[64:65], 3, s[20:21]
	global_load_dwordx2 v[64:65], v[64:65], off
.Lbs5_ld:
	s_or_b64 exec, exec, s[0:1]
	v_mov_b32_e32 v1, 2
	s_waitcnt vmcnt(0)
	v_lshlrev_b32_sdwa v11, v1, v9 dst_sel:DWORD dst_unused:UNUSED_PAD src0_sel:DWORD src1_sel:WORD_0
	v_lshlrev_b32_sdwa v12, v1, v9 dst_sel:DWORD dst_unused:UNUSED_PAD src0_sel:DWORD src1_sel:WORD_1
	global_load_dword v31, v11, s[28:29]
	global_load_dword v32, v12, s[28:29]
	v_mov_b32_e32 v29, 0
	v_mov_b32_e32 v33, 0
	s_and_saveexec_b64 s[0:1], s[30:31]
	v_lshrrev_b32_e32 v11, 14, v9
	v_and_b32_e32 v11, 0x1fc, v11
	v_mov_b32_e32 v12, 1
	ds_add_rtn_u32 v33, v11, v12
	s_or_b64 exec, exec, s[0:1]
	v_lshlrev_b32_sdwa v11, v1, v7 dst_sel:DWORD dst_unused:UNUSED_PAD src0_sel:DWORD src1_sel:WORD_0
	v_lshlrev_b32_sdwa v1, v1, v7 dst_sel:DWORD dst_unused:UNUSED_PAD src0_sel:DWORD src1_sel:WORD_1
	global_load_dword v28, v11, s[28:29]
	global_load_dword v30, v1, s[28:29]
	s_and_saveexec_b64 s[0:1], s[26:27]
	v_lshrrev_b32_e32 v1, 14, v7
	v_and_b32_e32 v1, 0x1fc, v1
	v_mov_b32_e32 v11, 1
	ds_add_rtn_u32 v29, v1, v11
	s_or_b64 exec, exec, s[0:1]
	v_mov_b32_e32 v1, 2
	v_lshlrev_b32_sdwa v11, v1, v5 dst_sel:DWORD dst_unused:UNUSED_PAD src0_sel:DWORD src1_sel:WORD_0
	v_lshlrev_b32_sdwa v12, v1, v5 dst_sel:DWORD dst_unused:UNUSED_PAD src0_sel:DWORD src1_sel:WORD_1
	global_load_dword v25, v11, s[28:29]
	global_load_dword v26, v12, s[28:29]
	v_mov_b32_e32 v21, 0
	v_mov_b32_e32 v27, 0
	s_and_saveexec_b64 s[0:1], s[24:25]
	v_lshrrev_b32_e32 v11, 14, v5
	v_and_b32_e32 v11, 0x1fc, v11
	v_mov_b32_e32 v12, 1
	ds_add_rtn_u32 v27, v11, v12
	s_or_b64 exec, exec, s[0:1]
	v_lshlrev_b32_sdwa v11, v1, v3 dst_sel:DWORD dst_unused:UNUSED_PAD src0_sel:DWORD src1_sel:WORD_0
	v_lshlrev_b32_sdwa v12, v1, v3 dst_sel:DWORD dst_unused:UNUSED_PAD src0_sel:DWORD src1_sel:WORD_1
	global_load_dword v1, v11, s[28:29]
	global_load_dword v24, v12, s[28:29]
	s_and_saveexec_b64 s[0:1], s[22:23]
	v_lshrrev_b32_e32 v11, 14, v3
	v_and_b32_e32 v11, 0x1fc, v11
	v_mov_b32_e32 v12, 1
	ds_add_rtn_u32 v21, v11, v12
	s_or_b64 exec, exec, s[0:1]
	v_mov_b32_e32 v12, 2
	v_lshlrev_b32_sdwa v11, v12, v65 dst_sel:DWORD dst_unused:UNUSED_PAD src0_sel:DWORD src1_sel:WORD_0
	v_lshlrev_b32_sdwa v12, v12, v65 dst_sel:DWORD dst_unused:UNUSED_PAD src0_sel:DWORD src1_sel:WORD_1
	global_load_dword v68, v11, s[28:29]
	global_load_dword v69, v12, s[28:29]
	v_mov_b32_e32 v70, 0
	s_and_saveexec_b64 s[0:1], s[50:51]
	v_lshrrev_b32_e32 v11, 14, v65
	v_and_b32_e32 v11, 0x1fc, v11
	v_mov_b32_e32 v12, 1
	ds_add_rtn_u32 v70, v11, v12
	s_or_b64 exec, exec, s[0:1]
	s_branch .LBB2_41

.LBB2_153:
	s_or_b64 exec, exec, s[8:9]
	s_and_saveexec_b64 s[8:9], s[50:51]
	s_cbranch_execz .Lbs5_153
	v_lshrrev_b32_e32 v66, 14, v65
	v_and_b32_e32 v66, 0x1fc, v66
	ds_read_b32 v66, v66 offset:512
	v_cmp_gt_f32_e32 vcc, 1.0, v64
	v_mov_b32_e32 v6, 0
	s_and_saveexec_b64 s[10:11], vcc
	s_cbranch_execz .Lbs5_152
	v_mul_f32_e32 v67, 0x40490fdb, v64
	s_brev_b32 s0, 18
	v_cmp_nlt_f32_e64 s[0:1], |v67|, s0
	s_and_saveexec_b64 s[4:5], s[0:1]
	s_xor_b64 s[12:13], exec, s[4:5]
	s_cbranch_execz .Lbs5_149
	v_and_b32_e32 v6, 0x7fffffff, v67
	v_lshrrev_b32_e32 v7, 23, v6
	v_add_u32_e32 v7, 0xffffff88, v7
	v_not_b32_e32 v8, 63
	v_cmp_lt_u32_e32 vcc, 63, v7
	v_and_b32_e32 v6, 0x7fffff, v6
	v_or_b32_e32 v22, 0x800000, v6
	v_cndmask_b32_e32 v8, 0, v8, vcc
	v_add_u32_e32 v7, v8, v7
	v_not_b32_e32 v8, 31
	v_cmp_lt_u32_e64 s[0:1], 31, v7
	s_mov_b32 s3, 0xfe5163ab
	s_nop 0
	v_cndmask_b32_e64 v9, 0, v8, s[0:1]
	v_add_u32_e32 v7, v9, v7
	v_cmp_lt_u32_e64 s[4:5], 31, v7
	v_mov_b32_e32 v9, 0
	s_nop 0
	v_cndmask_b32_e64 v8, 0, v8, s[4:5]
	v_add_u32_e32 v20, v8, v7
	v_mad_u64_u32 v[6:7], s[6:7], v22, s3, 0
	v_mov_b32_e32 v8, v7
	s_mov_b32 s3, 0x3c439041
	v_mad_u64_u32 v[10:11], s[6:7], v22, s3, v[8:9]
	v_mov_b32_e32 v8, v11
	s_mov_b32 s3, 0xdb629599
	v_mad_u64_u32 v[12:13], s[6:7], v22, s3, v[8:9]
	v_mov_b32_e32 v8, v13
	s_mov_b32 s3, 0xf534ddc0
	v_mad_u64_u32 v[14:15], s[6:7], v22, s3, v[8:9]
	v_mov_b32_e32 v8, v15
	s_mov_b32 s3, 0xfc2757d1
	v_mad_u64_u32 v[16:17], s[6:7], v22, s3, v[8:9]
	v_mov_b32_e32 v8, v17
	s_mov_b32 s3, 0x4e441529
	v_mad_u64_u32 v[18:19], s[6:7], v22, s3, v[8:9]
	v_mov_b32_e32 v8, v19
	s_mov_b32 s3, 0xa2f9836e
	v_mad_u64_u32 v[8:9], s[6:7], v22, s3, v[8:9]
	v_cndmask_b32_e32 v7, v18, v14, vcc
	v_cndmask_b32_e32 v8, v8, v16, vcc
	v_cndmask_b32_e32 v9, v9, v18, vcc
	v_cndmask_b32_e64 v11, v8, v7, s[0:1]
	v_cndmask_b32_e64 v8, v9, v8, s[0:1]
	v_cndmask_b32_e32 v9, v16, v12, vcc
	v_cndmask_b32_e64 v7, v7, v9, s[0:1]
	v_cndmask_b32_e32 v10, v14, v10, vcc
	v_cndmask_b32_e64 v8, v8, v11, s[4:5]
	v_cndmask_b32_e64 v11, v11, v7, s[4:5]
	v_sub_u32_e32 v13, 32, v20
	v_cndmask_b32_e64 v9, v9, v10, s[0:1]
	v_alignbit_b32 v15, v8, v11, v13
	v_cmp_eq_u32_e64 s[6:7], 0, v20
	v_cndmask_b32_e64 v7, v7, v9, s[4:5]
	v_alignbit_b32 v14, v11, v7, v13
	v_cndmask_b32_e64 v8, v15, v8, s[6:7]
	v_cndmask_b32_e32 v6, v12, v6, vcc
	v_cndmask_b32_e64 v11, v14, v11, s[6:7]
	v_bfe_u32 v16, v8, 29, 1
	v_cndmask_b32_e64 v6, v10, v6, s[0:1]
	v_alignbit_b32 v14, v8, v11, 30
	v_sub_u32_e32 v17, 0, v16
	v_cndmask_b32_e64 v6, v9, v6, s[4:5]
	v_xor_b32_e32 v14, v14, v17
	v_alignbit_b32 v9, v7, v6, v13
	v_cndmask_b32_e64 v7, v9, v7, s[6:7]
	v_ffbh_u32_e32 v10, v14
	v_alignbit_b32 v9, v11, v7, 30
	v_min_u32_e32 v10, 32, v10
	v_alignbit_b32 v6, v7, v6, 30
	v_xor_b32_e32 v9, v9, v17
	v_sub_u32_e32 v11, 31, v10
	v_xor_b32_e32 v6, v6, v17
	v_alignbit_b32 v12, v14, v9, v11
	v_alignbit_b32 v6, v9, v6, v11
	v_alignbit_b32 v7, v12, v6, 9
	v_ffbh_u32_e32 v9, v7
	v_min_u32_e32 v9, 32, v9
	v_lshrrev_b32_e32 v15, 29, v8
	v_not_b32_e32 v11, v9
	v_alignbit_b32 v6, v7, v6, v11
	v_lshlrev_b32_e32 v7, 31, v15
	v_or_b32_e32 v11, 0x33000000, v7
	v_add_lshl_u32 v9, v9, v10, 23
	v_lshrrev_b32_e32 v6, 9, v6
	v_sub_u32_e32 v9, v11, v9
	v_or_b32_e32 v7, 0.5, v7
	v_lshlrev_b32_e32 v10, 23, v10
	v_or_b32_e32 v6, v9, v6
	v_lshrrev_b32_e32 v9, 9, v12
	v_sub_u32_e32 v7, v7, v10
	v_or_b32_e32 v7, v9, v7
	s_mov_b32 s0, 0x3fc90fda
	v_mul_f32_e32 v9, 0x3fc90fda, v7
	v_fma_f32 v10, v7, s0, -v9
	v_fmamk_f32 v7, v7, 0x33a22168, v10
	v_fmac_f32_e32 v7, 0x3fc90fda, v6
	v_lshrrev_b32_e32 v6, 30, v8
	v_add_f32_e32 v7, v9, v7
	v_add_u32_e32 v6, v16, v6
.Lbs5_149:
	s_andn2_saveexec_b64 s[0:1], s[12:13]
	s_cbranch_execz .Lbs5_151
	s_mov_b32 s3, 0x3f22f983
	v_mul_f32_e64 v6, |v67|, s3
	v_rndne_f32_e32 v7, v6
	s_mov_b32 s3, 0xbfc90fda
	v_cvt_i32_f32_e32 v6, v7
	v_fma_f32 v8, v7, s3, |v67|
	v_fmamk_f32 v8, v7, 0xb3a22168, v8
	v_fmamk_f32 v7, v7, 0xa7c234c4, v8
.Lbs5_151:
	s_or_b64 exec, exec, s[0:1]
	v_mul_f32_e32 v8, v7, v7
	v_mov_b32_e32 v9, 0x3c0881c4
	v_fmac_f32_e32 v9, 0xb94c1982, v8
	v_fmaak_f32 v9, v8, v9, 0xbe2aaa9d
	v_mul_f32_e32 v9, v8, v9
	v_fmac_f32_e32 v7, v7, v9
	v_mov_b32_e32 v9, 0xbab64f3b
	v_fmac_f32_e32 v9, 0x37d75334, v8
	v_fmaak_f32 v9, v8, v9, 0x3d2aabf7
	v_fmaak_f32 v9, v8, v9, 0xbf000004
	v_fma_f32 v8, v8, v9, 1.0
	v_and_b32_e32 v9, 1, v6
	v_cmp_eq_u32_e32 vcc, 0, v9
	v_lshlrev_b32_e32 v6, 30, v6
	s_brev_b32 s0, 1
	v_cndmask_b32_e64 v7, -v7, v8, vcc
	v_bitop3_b32 v6, v6, v7, s0 bitop3:0x6c
	s_movk_i32 s0, 0x1f8
	v_add_f32_e32 v6, 1.0, v6
	v_mul_f32_e32 v6, 0.5, v6
	v_mov_b32_e32 v7, 0x7fc00000
	v_cmp_class_f32_e64 vcc, v67, s0
	s_nop 1
	v_cndmask_b32_e32 v6, v7, v6, vcc
.Lbs5_152:
	s_or_b64 exec, exec, s[10:11]
	s_waitcnt lgkmcnt(0)
	v_add3_u32 v66, v70, s14, v66
	v_and_b32_e32 v67, 0xffff0000, v65
	s_waitcnt vmcnt(0)
	v_lshl_or_b32 v7, v69, 8, v67
	v_lshlrev_b32_e32 v10, 16, v68
	v_ashrrev_i32_e32 v67, 31, v66
	v_lshl_add_u64 v[8:9], v[66:67], 4, s[16:17]
	v_or_b32_sdwa v67, v10, v65 dst_sel:DWORD dst_unused:UNUSED_PAD src0_sel:DWORD src1_sel:WORD_0
	v_or_b32_e32 v66, v7, v68
	v_mov_b32_e32 v65, v6
	global_store_dwordx4 v[8:9], v[64:67], off

	.amdhsa_kernel _Z7k_bsortPK15HIP_vector_typeIfLj2EEPKiS4_PS_IfLj4EEPi
		.amdhsa_group_segment_fixed_size 1024
		.amdhsa_private_segment_fixed_size 0
		.amdhsa_kernarg_size 40
		.amdhsa_user_sgpr_count 2
		.amdhsa_user_sgpr_dispatch_ptr 0
		.amdhsa_user_sgpr_queue_ptr 0
		.amdhsa_user_sgpr_kernarg_segment_ptr 1
		.amdhsa_user_sgpr_dispatch_id 0
		.amdhsa_user_sgpr_kernarg_preload_length 0
		.amdhsa_user_sgpr_kernarg_preload_offset 0
		.amdhsa_user_sgpr_private_segment_size 0
		.amdhsa_uses_dynamic_stack 0
		.amdhsa_enable_private_segment 0
		.amdhsa_system_sgpr_workgroup_id_x 1
		.amdhsa_system_sgpr_workgroup_id_y 0
		.amdhsa_system_sgpr_workgroup_id_z 0
		.amdhsa_system_sgpr_workgroup_info 0
		.amdhsa_system_vgpr_workitem_id 0
		.amdhsa_next_free_vgpr 71
		.amdhsa_next_free_sgpr 52
		.amdhsa_accum_offset 72
		.amdhsa_reserve_vcc 1
		.amdhsa_float_round_mode_32 0
		.amdhsa_float_round_mode_16_64 0
		.amdhsa_float_denorm_mode_32 3
		.amdhsa_float_denorm_mode_16_64 3
		.amdhsa_dx10_clamp 1
		.amdhsa_ieee_mode 1
		.amdhsa_fp16_overflow 0
		.amdhsa_tg_split 0
		.amdhsa_exception_fp_ieee_invalid_op 0
		.amdhsa_exception_fp_denorm_src 0
		.amdhsa_exception_fp_ieee_div_zero 0
		.amdhsa_exception_fp_ieee_overflow 0
		.amdhsa_exception_fp_ieee_underflow 0
		.amdhsa_exception_fp_ieee_inexact 0
		.amdhsa_exception_int_div_zero 0
	.end_amdhsa_kernel

amdhsa.kernels:
  - .agpr_count:     0
    .args:
      - .actual_access:  read_only
        .address_space:  global
        .offset:         0
        .size:           8
        .value_kind:     global_buffer
      - .actual_access:  write_only
        .address_space:  global
        .offset:         8
        .size:           8
        .value_kind:     global_buffer
      - .offset:         16
        .size:           288
        .value_kind:     by_value
      - .actual_access:  write_only
        .address_space:  global
        .offset:         304
        .size:           8
        .value_kind:     global_buffer
      - .actual_access:  write_only
        .address_space:  global
        .offset:         312
        .size:           8
        .value_kind:     global_buffer
    .group_segment_fixed_size: 1564
    .kernarg_segment_align: 8
    .kernarg_segment_size: 320
    .language:       OpenCL C
    .language_version:
      - 2
      - 0
    .max_flat_workgroup_size: 256
    .name:           _Z8k_bcountPKiPi8PrepArgsPDF16_S3_
    .private_segment_fixed_size: 0
    .sgpr_count:     26
    .sgpr_spill_count: 0
    .symbol:         _Z8k_bcountPKiPi8PrepArgsPDF16_S3_.kd
    .uniform_work_group_size: 1
    .uses_dynamic_stack: false
    .vgpr_count:     26
    .vgpr_spill_count: 0
    .wavefront_size: 64
  - .agpr_count:     0
    .args:
      - .actual_access:  read_only
        .address_space:  global
        .offset:         0
        .size:           8
        .value_kind:     global_buffer
      - .actual_access:  read_only
        .address_space:  global
        .offset:         8
        .size:           8
        .value_kind:     global_buffer
      - .actual_access:  read_only
        .address_space:  global
        .offset:         16
        .size:           8
        .value_kind:     global_buffer
      - .actual_access:  read_only
        .address_space:  global
        .offset:         24
        .size:           8
        .value_kind:     global_buffer
      - .actual_access:  write_only
        .address_space:  global
        .offset:         32
        .size:           8
        .value_kind:     global_buffer
      - .actual_access:  write_only
        .address_space:  global
        .offset:         40
        .size:           8
        .value_kind:     global_buffer
      - .actual_access:  write_only
        .address_space:  global
        .offset:         48
        .size:           8
        .value_kind:     global_buffer
    .group_segment_fixed_size: 19228
    .kernarg_segment_align: 8
    .kernarg_segment_size: 56
    .language:       OpenCL C
    .language_version:
      - 2
      - 0
    .max_flat_workgroup_size: 512
    .name:           _Z10k_bscatterPKfPKiS2_S2_PiP15HIP_vector_typeIfLj2EEPf
    .private_segment_fixed_size: 0
    .sgpr_count:     26
    .sgpr_spill_count: 0
    .symbol:         _Z10k_bscatterPKfPKiS2_S2_PiP15HIP_vector_typeIfLj2EEPf.kd
    .uniform_work_group_size: 1
    .uses_dynamic_stack: false
    .vgpr_count:     196
    .vgpr_spill_count: 0
    .wavefront_size: 64
  - .agpr_count:     0
    .args:
      - .actual_access:  read_only
        .address_space:  global
        .offset:         0
        .size:           8
        .value_kind:     global_buffer
      - .actual_access:  read_only
        .address_space:  global
        .offset:         8
        .size:           8
        .value_kind:     global_buffer
      - .actual_access:  read_only
        .address_space:  global
        .offset:         16
        .size:           8
        .value_kind:     global_buffer
      - .actual_access:  write_only
        .address_space:  global
        .offset:         24
        .size:           8
        .value_kind:     global_buffer
      - .actual_access:  write_only
        .address_space:  global
        .offset:         32
        .size:           8
        .value_kind:     global_buffer
    .group_segment_fixed_size: 1024
    .kernarg_segment_align: 8
    .kernarg_segment_size: 40
    .language:       OpenCL C
    .language_version:
      - 2
      - 0
    .max_flat_workgroup_size: 512
    .name:           _Z7k_bsortPK15HIP_vector_typeIfLj2EEPKiS4_PS_IfLj4EEPi
    .private_segment_fixed_size: 0
    .sgpr_count:     58
    .sgpr_spill_count: 0
    .symbol:         _Z7k_bsortPK15HIP_vector_typeIfLj2EEPKiS4_PS_IfLj4EEPi.kd
    .uniform_work_group_size: 1
    .uses_dynamic_stack: false
    .vgpr_count:     71
    .vgpr_spill_count: 0
    .wavefront_size: 64
  - .agpr_count:     0
    .args:
      - .actual_access:  read_only
        .address_space:  global
        .offset:         0
        .size:           8
        .value_kind:     global_buffer
      - .actual_access:  read_only
        .address_space:  global
        .offset:         8
        .size:           8
        .value_kind:     global_buffer
      - .actual_access:  read_only
        .address_space:  global
        .offset:         16
        .size:           8
        .value_kind:     global_buffer
      - .actual_access:  read_only
        .address_space:  global
        .offset:         24
        .size:           8
        .value_kind:     global_buffer
      - .actual_access:  read_only
        .address_space:  global
        .offset:         32
        .size:           8
        .value_kind:     global_buffer
      - .actual_access:  read_only
        .address_space:  global
        .offset:         40
        .size:           8
        .value_kind:     global_buffer
      - .actual_access:  write_only
        .address_space:  global
        .offset:         48
        .size:           8
        .value_kind:     global_buffer
      - .actual_access:  write_only
        .address_space:  global
        .offset:         56
        .size:           8
        .value_kind:     global_buffer
      - .offset:         64
        .size:           4
        .value_kind:     hidden_block_count_x
      - .offset:         68
        .size:           4
        .value_kind:     hidden_block_count_y
      - .offset:         72
        .size:           4
        .value_kind:     hidden_block_count_z
      - .offset:         76
        .size:           2
        .value_kind:     hidden_group_size_x
      - .offset:         78
        .size:           2
        .value_kind:     hidden_group_size_y
      - .offset:         80
        .size:           2
        .value_kind:     hidden_group_size_z
      - .offset:         82
        .size:           2
        .value_kind:     hidden_remainder_x
      - .offset:         84
        .size:           2
        .value_kind:     hidden_remainder_y
      - .offset:         86
        .size:           2
        .value_kind:     hidden_remainder_z
      - .offset:         104
        .size:           8
        .value_kind:     hidden_global_offset_x
      - .offset:         112
        .size:           8
        .value_kind:     hidden_global_offset_y
      - .offset:         120
        .size:           8
        .value_kind:     hidden_global_offset_z
      - .offset:         128
        .size:           2
        .value_kind:     hidden_grid_dims
    .group_segment_fixed_size: 31488
    .kernarg_segment_align: 8
    .kernarg_segment_size: 320
    .language:       OpenCL C
    .language_version:
      - 2
      - 0
    .max_flat_workgroup_size: 256
    .name:           _Z7k_edge0PK15HIP_vector_typeIfLj4EEPKDv8_DF16_S5_PKfS7_S7_PfS8_
    .private_segment_fixed_size: 0
    .sgpr_count:     59
    .sgpr_spill_count: 0
    .symbol:         _Z7k_edge0PK15HIP_vector_typeIfLj4EEPKDv8_DF16_S5_PKfS7_S7_PfS8_.kd
    .uniform_work_group_size: 1
    .uses_dynamic_stack: false
    .vgpr_count:     96
    .vgpr_spill_count: 0
    .wavefront_size: 64
  - .agpr_count:     0
    .args:
      - .actual_access:  read_only
        .address_space:  global
        .offset:         0
        .size:           8
        .value_kind:     global_buffer
      - .actual_access:  read_only
        .address_space:  global
        .offset:         8
        .size:           8
        .value_kind:     global_buffer
      - .actual_access:  read_only
        .address_space:  global
        .offset:         16
        .size:           8
        .value_kind:     global_buffer
      - .actual_access:  read_only
        .address_space:  global
        .offset:         24
        .size:           8
        .value_kind:     global_buffer
      - .actual_access:  read_only
        .address_space:  global
        .offset:         32
        .size:           8
        .value_kind:     global_buffer
      - .actual_access:  read_only
        .address_space:  global
        .offset:         40
        .size:           8
        .value_kind:     global_buffer
      - .address_space:  global
        .offset:         48
        .size:           8
        .value_kind:     global_buffer
      - .actual_access:  write_only
        .address_space:  global
        .offset:         56
        .size:           8
        .value_kind:     global_buffer
      - .actual_access:  write_only
        .address_space:  global
        .offset:         64
        .size:           8
        .value_kind:     global_buffer
      - .offset:         72
        .size:           4
        .value_kind:     hidden_block_count_x
      - .offset:         76
        .size:           4
        .value_kind:     hidden_block_count_y
      - .offset:         80
        .size:           4
        .value_kind:     hidden_block_count_z
      - .offset:         84
        .size:           2
        .value_kind:     hidden_group_size_x
      - .offset:         86
        .size:           2
        .value_kind:     hidden_group_size_y
      - .offset:         88
        .size:           2
        .value_kind:     hidden_group_size_z
      - .offset:         90
        .size:           2
        .value_kind:     hidden_remainder_x
      - .offset:         92
        .size:           2
        .value_kind:     hidden_remainder_y
      - .offset:         94
        .size:           2
        .value_kind:     hidden_remainder_z
      - .offset:         112
        .size:           8
        .value_kind:     hidden_global_offset_x
      - .offset:         120
        .size:           8
        .value_kind:     hidden_global_offset_y
      - .offset:         128
        .size:           8
        .value_kind:     hidden_global_offset_z
      - .offset:         136
        .size:           2
        .value_kind:     hidden_grid_dims
    .group_segment_fixed_size: 31488
    .kernarg_segment_align: 8
    .kernarg_segment_size: 328
    .language:       OpenCL C
    .language_version:
      - 2
      - 0
    .max_flat_workgroup_size: 256
    .name:           _Z7k_edge1PK15HIP_vector_typeIfLj4EEPKDv8_DF16_S5_PKfS7_S7_PKDv2_DF16_PfSB_
    .private_segment_fixed_size: 0
    .sgpr_count:     56
    .sgpr_spill_count: 0
    .symbol:         _Z7k_edge1PK15HIP_vector_typeIfLj4EEPKDv8_DF16_S5_PKfS7_S7_PKDv2_DF16_PfSB_.kd
    .uniform_work_group_size: 1
    .uses_dynamic_stack: false
    .vgpr_count:     128
    .vgpr_spill_count: 0
    .wavefront_size: 64
  - .agpr_count:     0
    .args:
      - .actual_access:  read_only
        .address_space:  global
        .offset:         0
        .size:           8
        .value_kind:     global_buffer
      - .actual_access:  read_only
        .address_space:  global
        .offset:         8
        .size:           8
        .value_kind:     global_buffer
      - .address_space:  global
        .offset:         16
        .size:           8
        .value_kind:     global_buffer
      - .address_space:  global
        .offset:         24
        .size:           8
        .value_kind:     global_buffer
    .group_segment_fixed_size: 0
    .kernarg_segment_align: 8
    .kernarg_segment_size: 32
    .language:       OpenCL C
    .language_version:
      - 2
      - 0
    .max_flat_workgroup_size: 256
    .name:           _Z6k_poolPKfPKiPfS3_
    .private_segment_fixed_size: 0
    .sgpr_count:     20
    .sgpr_spill_count: 0
    .symbol:         _Z6k_poolPKfPKiPfS3_.kd
    .uniform_work_group_size: 1
    .uses_dynamic_stack: false
    .vgpr_count:     16
    .vgpr_spill_count: 0
    .wavefront_size: 64
  - .agpr_count:     0
    .args:
      - .actual_access:  read_only
        .address_space:  global
        .offset:         0
        .size:           8
        .value_kind:     global_buffer
      - .actual_access:  read_only
        .address_space:  global
        .offset:         8
        .size:           8
        .value_kind:     global_buffer
      - .actual_access:  read_only
        .address_space:  global
        .offset:         16
        .size:           8
        .value_kind:     global_buffer
      - .actual_access:  read_only
        .address_space:  global
        .offset:         24
        .size:           8
        .value_kind:     global_buffer
      - .actual_access:  read_only
        .address_space:  global
        .offset:         32
        .size:           8
        .value_kind:     global_buffer
      - .actual_access:  read_only
        .address_space:  global
        .offset:         40
        .size:           8
        .value_kind:     global_buffer
      - .actual_access:  write_only
        .address_space:  global
        .offset:         48
        .size:           8
        .value_kind:     global_buffer
    .group_segment_fixed_size: 20480
    .kernarg_segment_align: 8
    .kernarg_segment_size: 56
    .language:       OpenCL C
    .language_version:
      - 2
      - 0
    .max_flat_workgroup_size: 64
    .name:           _Z7k_finalPKfS0_S0_S0_S0_S0_Pf
    .private_segment_fixed_size: 0
    .sgpr_count:     42
    .sgpr_spill_count: 0
    .symbol:         _Z7k_finalPKfS0_S0_S0_S0_S0_Pf.kd
    .uniform_work_group_size: 1
    .uses_dynamic_stack: false
    .vgpr_count:     144
    .vgpr_spill_count: 0
    .wavefront_size: 64
  - .agpr_count:     0
    .args:
      - .actual_access:  read_only
        .address_space:  global
        .offset:         0
        .size:           8
        .value_kind:     global_buffer
      - .address_space:  global
        .offset:         8
        .size:           8
        .value_kind:     global_buffer
      - .address_space:  global
        .offset:         16
        .size:           8
        .value_kind:     global_buffer
      - .actual_access:  read_only
        .address_space:  global
        .offset:         24
        .size:           8
        .value_kind:     global_buffer
      - .actual_access:  read_only
        .address_space:  global
        .offset:         32
        .size:           8
        .value_kind:     global_buffer
      - .actual_access:  read_only
        .address_space:  global
        .offset:         40
        .size:           8
        .value_kind:     global_buffer
      - .actual_access:  read_only
        .address_space:  global
        .offset:         48
        .size:           8
        .value_kind:     global_buffer
      - .actual_access:  read_only
        .address_space:  global
        .offset:         56
        .size:           8
        .value_kind:     global_buffer
      - .actual_access:  read_only
        .address_space:  global
        .offset:         64
        .size:           8
        .value_kind:     global_buffer
      - .actual_access:  read_only
        .address_space:  global
        .offset:         72
        .size:           8
        .value_kind:     global_buffer
      - .actual_access:  read_only
        .address_space:  global
        .offset:         80
        .size:           8
        .value_kind:     global_buffer
      - .actual_access:  read_only
        .address_space:  global
        .offset:         88
        .size:           8
        .value_kind:     global_buffer
      - .actual_access:  read_only
        .address_space:  global
        .offset:         96
        .size:           8
        .value_kind:     global_buffer
      - .actual_access:  read_only
        .address_space:  global
        .offset:         104
        .size:           8
        .value_kind:     global_buffer
      - .actual_access:  read_only
        .address_space:  global
        .offset:         112
        .size:           8
        .value_kind:     global_buffer
    .group_segment_fixed_size: 59392
    .kernarg_segment_align: 8
    .kernarg_segment_size: 120
    .language:       OpenCL C
    .language_version:
      - 2
      - 0
    .max_flat_workgroup_size: 256
    .name:           _Z6k_nodeILi0ELi0EEvPfS0_PDv2_DF16_PKiPKfS4_S0_S0_S4_S6_PKDv8_DF16_S6_S9_S6_S9_
    .private_segment_fixed_size: 0
    .sgpr_count:     30
    .sgpr_spill_count: 0
    .symbol:         _Z6k_nodeILi0ELi0EEvPfS0_PDv2_DF16_PKiPKfS4_S0_S0_S4_S6_PKDv8_DF16_S6_S9_S6_S9_.kd
    .uniform_work_group_size: 1
    .uses_dynamic_stack: false
    .vgpr_count:     154
    .vgpr_spill_count: 0
    .wavefront_size: 64
  - .agpr_count:     0
    .args:
      - .actual_access:  read_only
        .address_space:  global
        .offset:         0
        .size:           8
        .value_kind:     global_buffer
      - .address_space:  global
        .offset:         8
        .size:           8
        .value_kind:     global_buffer
      - .address_space:  global
        .offset:         16
        .size:           8
        .value_kind:     global_buffer
      - .actual_access:  read_only
        .address_space:  global
        .offset:         24
        .size:           8
        .value_kind:     global_buffer
      - .actual_access:  read_only
        .address_space:  global
        .offset:         32
        .size:           8
        .value_kind:     global_buffer
      - .actual_access:  read_only
        .address_space:  global
        .offset:         40
        .size:           8
        .value_kind:     global_buffer
      - .actual_access:  read_only
        .address_space:  global
        .offset:         48
        .size:           8
        .value_kind:     global_buffer
      - .actual_access:  read_only
        .address_space:  global
        .offset:         56
        .size:           8
        .value_kind:     global_buffer
      - .actual_access:  read_only
        .address_space:  global
        .offset:         64
        .size:           8
        .value_kind:     global_buffer
      - .actual_access:  read_only
        .address_space:  global
        .offset:         72
        .size:           8
        .value_kind:     global_buffer
      - .actual_access:  read_only
        .address_space:  global
        .offset:         80
        .size:           8
        .value_kind:     global_buffer
      - .actual_access:  read_only
        .address_space:  global
        .offset:         88
        .size:           8
        .value_kind:     global_buffer
      - .actual_access:  read_only
        .address_space:  global
        .offset:         96
        .size:           8
        .value_kind:     global_buffer
      - .actual_access:  read_only
        .address_space:  global
        .offset:         104
        .size:           8
        .value_kind:     global_buffer
      - .actual_access:  read_only
        .address_space:  global
        .offset:         112
        .size:           8
        .value_kind:     global_buffer
    .group_segment_fixed_size: 59392
    .kernarg_segment_align: 8
    .kernarg_segment_size: 120
    .language:       OpenCL C
    .language_version:
      - 2
      - 0
    .max_flat_workgroup_size: 256
    .name:           _Z6k_nodeILi1ELi0EEvPfS0_PDv2_DF16_PKiPKfS4_S0_S0_S4_S6_PKDv8_DF16_S6_S9_S6_S9_
    .private_segment_fixed_size: 0
    .sgpr_count:     30
    .sgpr_spill_count: 0
    .symbol:         _Z6k_nodeILi1ELi0EEvPfS0_PDv2_DF16_PKiPKfS4_S0_S0_S4_S6_PKDv8_DF16_S6_S9_S6_S9_.kd
    .uniform_work_group_size: 1
    .uses_dynamic_stack: false
    .vgpr_count:     220
    .vgpr_spill_count: 0
    .wavefront_size: 64
  - .agpr_count:     0
    .args:
      - .actual_access:  read_only
        .address_space:  global
        .offset:         0
        .size:           8
        .value_kind:     global_buffer
      - .actual_access:  read_only
        .address_space:  global
        .offset:         8
        .size:           8
        .value_kind:     global_buffer
      - .address_space:  global
        .offset:         16
        .size:           8
        .value_kind:     global_buffer
      - .actual_access:  read_only
        .address_space:  global
        .offset:         24
        .size:           8
        .value_kind:     global_buffer
      - .actual_access:  read_only
        .address_space:  global
        .offset:         32
        .size:           8
        .value_kind:     global_buffer
      - .actual_access:  read_only
        .address_space:  global
        .offset:         40
        .size:           8
        .value_kind:     global_buffer
      - .address_space:  global
        .offset:         48
        .size:           8
        .value_kind:     global_buffer
      - .address_space:  global
        .offset:         56
        .size:           8
        .value_kind:     global_buffer
      - .actual_access:  read_only
        .address_space:  global
        .offset:         64
        .size:           8
        .value_kind:     global_buffer
      - .actual_access:  read_only
        .address_space:  global
        .offset:         72
        .size:           8
        .value_kind:     global_buffer
      - .actual_access:  read_only
        .address_space:  global
        .offset:         80
        .size:           8
        .value_kind:     global_buffer
      - .actual_access:  read_only
        .address_space:  global
        .offset:         88
        .size:           8
        .value_kind:     global_buffer
      - .actual_access:  read_only
        .address_space:  global
        .offset:         96
        .size:           8
        .value_kind:     global_buffer
      - .actual_access:  read_only
        .address_space:  global
        .offset:         104
        .size:           8
        .value_kind:     global_buffer
      - .actual_access:  read_only
        .address_space:  global
        .offset:         112
        .size:           8
        .value_kind:     global_buffer
    .group_segment_fixed_size: 59392
    .kernarg_segment_align: 8
    .kernarg_segment_size: 120
    .language:       OpenCL C
    .language_version:
      - 2
      - 0
    .max_flat_workgroup_size: 256
    .name:           _Z6k_nodeILi1ELi1EEvPfS0_PDv2_DF16_PKiPKfS4_S0_S0_S4_S6_PKDv8_DF16_S6_S9_S6_S9_
    .private_segment_fixed_size: 0
    .sgpr_count:     30
    .sgpr_spill_count: 0
    .symbol:         _Z6k_nodeILi1ELi1EEvPfS0_PDv2_DF16_PKiPKfS4_S0_S0_S4_S6_PKDv8_DF16_S6_S9_S6_S9_.kd
    .uniform_work_group_size: 1
    .uses_dynamic_stack: false
    .vgpr_count:     220
    .vgpr_spill_count: 0
    .wavefront_size: 64
